# T3a: three workgroup barriers per item removed (mid stage H, end of item, G to G') that order nothing
# speedup vs baseline: 1.0238x; 1.0235x over previous
; #define CK_BAR() do { asm volatile("s_waitcnt lgkmcnt(0)" ::: "memory"); __builtin_amdgcn_s_barrier(); asm volatile("" ::: "memory"); } while (0)
; __device__ __forceinline__ void phase1(const int WID_, const In& I, char* lds) {
;     ...
;             const bool frag = kind < 2;
;             *(uint2*)(dbase + 0) = w[0];
;             *(uint2*)(dbase + (frag ? 128 : 8)) = w[1];
;             *(uint2*)(dbase + (frag ? 1024 : 16)) = w[2];
;             *(uint2*)(dbase + (frag ? 1152 : 24)) = w[3];
;         }
;         CK_BAR();
.LBB0_1413:
	v_cvt_pk_bf16_f32 v0, v0, v1
	v_cvt_pk_bf16_f32 v1, v2, v3
	v_cvt_pk_bf16_f32 v2, v4, v5
	v_cvt_pk_bf16_f32 v3, v6, v7
	v_cvt_pk_bf16_f32 v4, v8, v9
	v_cvt_pk_bf16_f32 v5, v10, v11
	v_cvt_pk_bf16_f32 v6, v12, v13
	v_cvt_pk_bf16_f32 v7, v14, v15
	global_store_dwordx2 v[72:73], v[0:1], off
	global_store_dwordx2 v[72:73], v[2:3], off offset:16
	global_store_dwordx2 v[72:73], v[4:5], off offset:32
	global_store_dwordx2 v[72:73], v[6:7], off offset:48
	s_waitcnt lgkmcnt(0)
	s_cmpk_lt_i32 s33, 0x2000
	s_mov_b32 s40, s33
	s_cbranch_scc0 .LBB0_1473

; #define CK_BAR() do { asm volatile("s_waitcnt lgkmcnt(0)" ::: "memory"); __builtin_amdgcn_s_barrier(); asm volatile("" ::: "memory"); } while (0)
; __device__ __forceinline__ f32x16 zero16() { return (f32x16){0.f, 0.f, 0.f, 0.f, 0.f, 0.f, 0.f, 0.f, 0.f, 0.f, 0.f, 0.f, 0.f, 0.f, 0.f, 0.f}; }
; __device__ __forceinline__ void phase1(const int WID_, const In& I, char* lds) {
;     ...
;         if (wv == 0) { f32x16 acc = mm_tile<32>(zero16(), MAT(O_NM) + 32 * LD, LD, MAT(O_TT), 40, lane); store_tr(acc, MAT(O_ZT), 40, lane); }
;         CK_BAR();
;         if (wv == 0) { f32x16 acc = mm_tile<32>(zero16(), MAT(O_TM) + 32 * LD + 32, LD, MAT(O_ZT), 40, lane); store_rm(acc, MAT(O_TM) + 32 * LD, LD, lane); }
.LBB0_1456:
	s_waitcnt lgkmcnt(0)
	v_readlane_b32 s0, v243, 3
	v_readlane_b32 s1, v243, 4
	s_andn2_b64 vcc, exec, s[0:1]
	s_mov_b64 s[0:1], -1
	s_cbranch_vccnz .LBB0_1458
	v_and_b32_e32 v0, -8, v57
	v_and_b32_e32 v58, -4, v56
	s_mov_b64 s[0:1], 0

; #define CK_BAR() do { asm volatile("s_waitcnt lgkmcnt(0)" ::: "memory"); __builtin_amdgcn_s_barrier(); asm volatile("" ::: "memory"); } while (0)
; __device__ __forceinline__ unsigned cvtpk(float lo, float hi) { const f32x2_t v = {lo, hi}; const bf16x2_t b = __builtin_convertvector(v, bf16x2_t); return __builtin_bit_cast(unsigned, b); }
; __device__ __forceinline__ f32x16 zero16() { return (f32x16){0.f, 0.f, 0.f, 0.f, 0.f, 0.f, 0.f, 0.f, 0.f, 0.f, 0.f, 0.f, 0.f, 0.f, 0.f, 0.f}; }
; __device__ __forceinline__ void phase1(const int WID_, const In& I, char* lds) {
;     ...
;         { const int st = wv >> 2, ct = wv & 3;
;           f32x16 acc = mm_tile<64>(zero16(), MAT(O_TM) + 32 * st * LD, LD, MAT(O_AT) + 32 * ct * LD, LD, lane);
;           CK_BAR();
;           store_tr(acc, MAT(O_X1T) + 32 * ct * LD + 32 * st, LD, lane); }
;         CK_BAR();
;     ...
;             } else {
;                 f32x16 acc = mm_tile<64>(zero16(), MAT(O_X1T) + 32 * t0 * LD, LD, MAT(O_ARB) + 32 * t1 * LD, LD, lane);
;                 const int sq = 32 * t1 + cc;
;                 dbase = (bf16*)(out + 8192) + sq * 64 + 32 * t0 + 4 * hh;
;                 const bf16* rb = MAT(O_RB) + sq * LD + 32 * t0;
; #pragma unroll
;                 for (int g = 0; g < 4; ++g) { const uint2 rr = *(const uint2*)(rb + 8 * g + 4 * hh);
;                     const float x0 = acc[4 * g] + __builtin_bit_cast(float, rr.x << 16), x1 = acc[4 * g + 1] + __builtin_bit_cast(float, rr.x & 0xffff0000u);
;                     const float x2 = acc[4 * g + 2] + __builtin_bit_cast(float, rr.y << 16), x3 = acc[4 * g + 3] + __builtin_bit_cast(float, rr.y & 0xffff0000u);
;                     w[g].x = cvtpk(x0, x1); w[g].y = cvtpk(x2, x3); }
.LBB0_1460:
	v_lshlrev_b32_e32 v86, 1, v53
	v_lshlrev_b32_e32 v87, 1, v0
	s_waitcnt lgkmcnt(0)
	s_barrier
	v_add3_u32 v53, s53, v86, v87
	ds_read_b128 v[0:3], v53
	v_add3_u32 v68, s58, v86, v87
	ds_read_b128 v[4:7], v68 offset:36864
	ds_read_b128 v[54:57], v53 offset:32
	ds_read_b128 v[60:63], v68 offset:36896
	ds_read_b128 v[64:67], v53 offset:64
	v_lshlrev_b32_e32 v58, 1, v58
	s_waitcnt lgkmcnt(3)
	v_mfma_f32_32x32x16_bf16 v[0:15], v[0:3], v[4:7], 0
	s_ashr_i32 s41, s40, 31
	s_lshl_b64 s[0:1], s[40:41], 15
	v_or_b32_e32 v81, s62, v78
	s_add_u32 s0, s90, s0
	s_addc_u32 s1, s91, s1
	s_add_i32 s4, 0, 0x18c00
	v_add3_u32 v85, s4, v86, v87
	s_waitcnt lgkmcnt(1)
	v_mfma_f32_32x32x16_bf16 v[0:15], v[54:57], v[60:63], v[0:15]
	ds_read_b128 v[54:57], v68 offset:36928
	v_add3_u32 v62, s59, v86, v58
	ds_read_b128 v[58:61], v53 offset:96
	ds_read_b128 v[70:73], v68 offset:36960
	v_add_u32_e32 v53, 0x4800, v62
	v_lshlrev_b32_e32 v68, 7, v81
	s_waitcnt lgkmcnt(2)
	v_mfma_f32_32x32x16_bf16 v[0:15], v[64:67], v[54:57], v[0:15]
	s_lshl_b32 s4, s60, 1
	v_add3_u32 v82, 0, v86, v87
	s_mov_b64 s[6:7], 0x2000
	s_and_b64 vcc, exec, s[20:21]
	v_add_u32_e32 v88, s61, v82
	s_waitcnt lgkmcnt(0)
	v_mfma_f32_32x32x16_bf16 v[0:15], v[58:61], v[70:73], v[0:15]
	s_nop 11
	v_cvt_pk_bf16_f32 v0, v0, v1
	v_cvt_pk_bf16_f32 v1, v2, v3
	v_cvt_pk_bf16_f32 v2, v4, v5
	v_cvt_pk_bf16_f32 v3, v6, v7
	v_cvt_pk_bf16_f32 v4, v8, v9
	v_cvt_pk_bf16_f32 v5, v10, v11
	v_cvt_pk_bf16_f32 v6, v12, v13
	v_cvt_pk_bf16_f32 v7, v14, v15
	ds_write2_b64 v53, v[0:1], v[2:3] offset1:2
	ds_write2_b64 v53, v[4:5], v[6:7] offset0:4 offset1:6
	v_lshl_add_u64 v[0:1], s[0:1], 0, v[68:69]
	s_waitcnt lgkmcnt(0)
	s_barrier
	v_ashrrev_i32_e32 v53, 31, v52
	v_lshl_add_u64 v[0:1], v[0:1], 0, s[4:5]
	v_lshl_add_u64 v[70:71], v[52:53], 1, v[0:1]
	v_mul_u32_u24_e32 v0, 0x90, v81
	v_lshlrev_b32_e32 v1, 3, v79
	s_add_i32 s4, 0, 0x21400
	v_lshl_add_u64 v[72:73], v[70:71], 0, s[6:7]
	v_add3_u32 v84, s66, v0, v1
	v_lshl_add_u32 v83, v81, 2, s4
	v_add_u32_e32 v68, s60, v52
	s_mov_b64 s[6:7], -1
	s_cbranch_vccz .LBB0_1466
	ds_read_b128 v[64:67], v88 offset:18432
	ds_read_b128 v[60:63], v88 offset:18464
	ds_read_b128 v[56:59], v88 offset:18496
	ds_read_b128 v[52:55], v88 offset:18528
	s_and_b64 vcc, exec, s[22:23]
	s_cbranch_vccz .LBB0_1463
	v_add_u32_e32 v4, s63, v85
	ds_read_b128 v[0:3], v4
	ds_read_b128 v[90:93], v4 offset:32
	ds_read_b128 v[94:97], v4 offset:64
	ds_read_b128 v[98:101], v4 offset:96
	v_add_u32_e32 v74, 0x2000, v84
	s_waitcnt lgkmcnt(3)
	v_mfma_f32_32x32x16_bf16 v[0:15], v[64:67], v[0:3], 0
	s_mov_b64 s[6:7], 0
	s_waitcnt lgkmcnt(2)
	v_mfma_f32_32x32x16_bf16 v[0:15], v[60:63], v[90:93], v[0:15]
	s_waitcnt lgkmcnt(1)
	v_mfma_f32_32x32x16_bf16 v[0:15], v[56:59], v[94:97], v[0:15]
	ds_read2_b64 v[90:93], v74 offset0:128 offset1:130
	ds_read2_b64 v[94:97], v74 offset0:132 offset1:134
	s_waitcnt lgkmcnt(1)
	v_lshlrev_b32_e32 v74, 16, v90
	v_and_b32_e32 v75, 0xffff0000, v90
	v_mfma_f32_32x32x16_bf16 v[0:15], v[52:55], v[98:101], v[0:15]
	s_nop 11
	v_pk_add_f32 v[0:1], v[0:1], v[74:75]
	v_lshlrev_b32_e32 v74, 16, v91
	v_and_b32_e32 v75, 0xffff0000, v91
	v_pk_add_f32 v[2:3], v[2:3], v[74:75]
	v_lshlrev_b32_e32 v74, 16, v92
	v_and_b32_e32 v75, 0xffff0000, v92
	v_pk_add_f32 v[4:5], v[4:5], v[74:75]
	v_lshlrev_b32_e32 v74, 16, v93
	v_and_b32_e32 v75, 0xffff0000, v93
	v_pk_add_f32 v[6:7], v[6:7], v[74:75]
	s_waitcnt lgkmcnt(0)
	v_lshlrev_b32_e32 v74, 16, v94
	v_and_b32_e32 v75, 0xffff0000, v94
	v_pk_add_f32 v[8:9], v[8:9], v[74:75]
	v_lshlrev_b32_e32 v74, 16, v95
	v_and_b32_e32 v75, 0xffff0000, v95
	v_pk_add_f32 v[10:11], v[10:11], v[74:75]
	v_lshlrev_b32_e32 v74, 16, v96
	v_and_b32_e32 v75, 0xffff0000, v96
	v_pk_add_f32 v[12:13], v[12:13], v[74:75]
	v_lshlrev_b32_e32 v74, 16, v97
	v_and_b32_e32 v75, 0xffff0000, v97
	v_pk_add_f32 v[14:15], v[14:15], v[74:75]
